# grid barrier: all workgroups poll the cross-XCC arrival counter TOP directly (>= target) instead of the TOPGEN generation word; dead XGEN/TOPGEN adds removed
# speedup vs baseline: 1.0127x; 1.0049x over previous
; __device__ __forceinline__ unsigned xb_ld(unsigned* p)              { return __hip_atomic_load(p, __ATOMIC_RELAXED, __HIP_MEMORY_SCOPE_AGENT); }
; __device__ __forceinline__ unsigned xb_add(unsigned* p, unsigned v) { return __hip_atomic_fetch_add(p, v, __ATOMIC_RELAXED, __HIP_MEMORY_SCOPE_AGENT); }
; #define XB_SPIN(cond, bar) do { unsigned _sp = 0; while (cond) { __builtin_amdgcn_s_sleep(1); \
;     if ((++_sp & 255u) == 0u) { if (xb_ld(&(bar)[XB_TMO])) break; if (_sp > XB_SPIN_CAP) { atomicAdd(&(bar)[XB_TMO], 1u); break; } } } } while (0)
; __device__ __forceinline__ void xcd_barrier(const XcdBarrier& b, const bool xb_leader) {
;     ...
;         const unsigned old = xb_add(&bar[XB_XSUB(b.x)], 1u);
;         const unsigned gen = old / nloc;
;         if (old + 1u == (gen + 1u) * nloc) {
;             __builtin_amdgcn_fence(__ATOMIC_RELEASE, "agent");
;             asm volatile("s_waitcnt vmcnt(0)" ::: "memory");
;             const unsigned og = xb_add(&bar[XB_TOP], 1u);
;             const unsigned tg = og / nx;
;             if (og + 1u == (tg + 1u) * nx) xb_add(&bar[XB_TOPGEN], 1u);
;             else XB_SPIN(xb_ld(&bar[XB_TOPGEN]) == tg, bar);
;             __builtin_amdgcn_fence(__ATOMIC_ACQUIRE, "agent");
;             xb_add(&bar[XB_XGEN(b.x)], 1u);
;             asm volatile("s_waitcnt vmcnt(0)" ::: "memory");
;         } else {
;             XB_SPIN(xb_ld(&bar[XB_XGEN(b.x)]) == gen, bar);
.LBB0_87:
	s_or_b64 exec, exec, s[12:13]
	v_cvt_f32_u32_e32 v2, v9
	s_waitcnt vmcnt(0)
	v_readfirstlane_b32 s3, v1
	v_sub_u32_e32 v1, 0, v9
	v_rcp_iflag_f32_e32 v2, v2
	v_add_u32_e32 v3, s3, v0
	v_mul_f32_e32 v2, 0x4f7ffffe, v2
	v_cvt_u32_f32_e32 v2, v2
	v_mul_lo_u32 v0, v1, v2
	v_mul_hi_u32 v0, v2, v0
	v_add_u32_e32 v0, v2, v0
	v_mul_hi_u32 v0, v3, v0
	v_mul_lo_u32 v1, v0, v9
	v_sub_u32_e32 v1, v3, v1
	v_add_u32_e32 v2, 1, v0
	v_cmp_ge_u32_e32 vcc, v1, v9
	s_nop 1
	v_cndmask_b32_e32 v0, v0, v2, vcc
	v_sub_u32_e32 v2, v1, v9
	v_cndmask_b32_e32 v1, v1, v2, vcc
	v_add_u32_e32 v2, 1, v0
	v_cmp_ge_u32_e32 vcc, v1, v9
	v_add_u32_e32 v1, 1, v3
	s_nop 0
	v_cndmask_b32_e32 v0, v0, v2, vcc
	v_mul_lo_u32 v2, v9, v0
	v_add_u32_e32 v2, v2, v9
	v_cmp_ne_u32_e32 vcc, v1, v2
	s_and_saveexec_b64 s[6:7], vcc
	s_xor_b64 s[6:7], exec, s[6:7]
	s_cbranch_execz .LBB0_101
	s_waitcnt lgkmcnt(0)
	v_add_u32_e32 v0, 1, v0
	v_mul_lo_u32 v0, v0, v8
	v_mov_b32_e32 v1, 0x3000
	global_load_dword v1, v1, s[28:29] offset:1024 sc1
	s_add_u32 s14, s28, 0x3400
	s_addc_u32 s15, s29, 0
	s_waitcnt vmcnt(0)
	v_cmp_lt_u32_e32 vcc, v1, v0
	s_and_saveexec_b64 s[12:13], vcc
	s_cbranch_execz .LBB0_100
	s_mov_b32 s3, 1
	s_mov_b64 s[16:17], 0
	v_mov_b32_e32 v1, 0
	s_branch .LBB0_91

; __device__ __forceinline__ unsigned xb_ld(unsigned* p)              { return __hip_atomic_load(p, __ATOMIC_RELAXED, __HIP_MEMORY_SCOPE_AGENT); }
; #define XB_SPIN(cond, bar) do { unsigned _sp = 0; while (cond) { __builtin_amdgcn_s_sleep(1); \
;     if ((++_sp & 255u) == 0u) { if (xb_ld(&(bar)[XB_TMO])) break; if (_sp > XB_SPIN_CAP) { atomicAdd(&(bar)[XB_TMO], 1u); break; } } } } while (0)
; __device__ __forceinline__ void xcd_barrier(const XcdBarrier& b, const bool xb_leader) {
;     ...
;             XB_SPIN(xb_ld(&bar[XB_XGEN(b.x)]) == gen, bar);
.LBB0_95:
	global_load_dword v2, v1, s[14:15] sc1
	s_add_i32 s3, s3, 1
	s_mov_b64 s[22:23], -1
	s_waitcnt vmcnt(0)
	v_cmp_ge_u32_e32 vcc, v2, v0
	s_orn2_b64 s[20:21], vcc, exec
	s_branch .LBB0_90

; __device__ __forceinline__ unsigned xb_ld(unsigned* p)              { return __hip_atomic_load(p, __ATOMIC_RELAXED, __HIP_MEMORY_SCOPE_AGENT); }
; __device__ __forceinline__ unsigned xb_add(unsigned* p, unsigned v) { return __hip_atomic_fetch_add(p, v, __ATOMIC_RELAXED, __HIP_MEMORY_SCOPE_AGENT); }
; #define XB_SPIN(cond, bar) do { unsigned _sp = 0; while (cond) { __builtin_amdgcn_s_sleep(1); \
;     if ((++_sp & 255u) == 0u) { if (xb_ld(&(bar)[XB_TMO])) break; if (_sp > XB_SPIN_CAP) { atomicAdd(&(bar)[XB_TMO], 1u); break; } } } } while (0)
; __device__ __forceinline__ void xcd_barrier(const XcdBarrier& b, const bool xb_leader) {
;     ...
;             const unsigned og = xb_add(&bar[XB_TOP], 1u);
;             const unsigned tg = og / nx;
;             if (og + 1u == (tg + 1u) * nx) xb_add(&bar[XB_TOPGEN], 1u);
;             else XB_SPIN(xb_ld(&bar[XB_TOPGEN]) == tg, bar);
.LBB0_104:
	s_or_b64 exec, exec, s[12:13]
	v_cvt_f32_u32_e32 v2, v8
	s_waitcnt vmcnt(0)
	v_readfirstlane_b32 s3, v1
	s_add_u32 s12, s28, 0x3400
	s_addc_u32 s13, s29, 0
	v_rcp_iflag_f32_e32 v2, v2
	v_add_u32_e32 v0, s3, v0
	v_add_u32_e32 v3, 1, v0
	s_mov_b64 s[14:15], 0
	v_mul_f32_e32 v1, 0x4f7ffffe, v2
	v_cvt_u32_f32_e32 v1, v1
	v_sub_u32_e32 v2, 0, v8
	v_mul_lo_u32 v2, v2, v1
	v_mul_hi_u32 v2, v1, v2
	v_add_u32_e32 v1, v1, v2
	v_mul_hi_u32 v1, v0, v1
	v_mul_lo_u32 v2, v1, v8
	v_sub_u32_e32 v0, v0, v2
	v_add_u32_e32 v4, 1, v1
	v_cmp_ge_u32_e32 vcc, v0, v8
	v_sub_u32_e32 v2, v0, v8
	s_nop 0
	v_cndmask_b32_e32 v1, v1, v4, vcc
	v_cndmask_b32_e32 v0, v0, v2, vcc
	v_add_u32_e32 v2, 1, v1
	v_cmp_ge_u32_e32 vcc, v0, v8
	s_nop 1
	v_cndmask_b32_e32 v2, v1, v2, vcc
	v_mul_lo_u32 v0, v8, v2
	v_add_u32_e32 v0, v0, v8
	v_cmp_ne_u32_e32 vcc, v3, v0
	v_mov_b32_e32 v4, v0
	v_mov_b64_e32 v[0:1], s[12:13]
	s_and_saveexec_b64 s[6:7], vcc
	s_cbranch_execz .LBB0_116
	v_mov_b32_e32 v0, 0
	global_load_dword v1, v0, s[12:13] sc1
	s_mov_b64 s[18:19], 0
	s_waitcnt vmcnt(0)
	v_cmp_lt_u32_e32 vcc, v1, v4
	s_and_saveexec_b64 s[16:17], vcc
	s_cbranch_execz .LBB0_115
	s_add_u32 s14, s28, 0x200
	s_addc_u32 s15, s29, 0
	s_mov_b32 s3, 1
	s_branch .LBB0_108

; __device__ __forceinline__ unsigned xb_ld(unsigned* p)              { return __hip_atomic_load(p, __ATOMIC_RELAXED, __HIP_MEMORY_SCOPE_AGENT); }
; #define XB_SPIN(cond, bar) do { unsigned _sp = 0; while (cond) { __builtin_amdgcn_s_sleep(1); \
;     if ((++_sp & 255u) == 0u) { if (xb_ld(&(bar)[XB_TMO])) break; if (_sp > XB_SPIN_CAP) { atomicAdd(&(bar)[XB_TMO], 1u); break; } } } } while (0)
; __device__ __forceinline__ void xcd_barrier(const XcdBarrier& b, const bool xb_leader) {
;     ...
;             else XB_SPIN(xb_ld(&bar[XB_TOPGEN]) == tg, bar);
.LBB0_112:
	global_load_dword v1, v0, s[12:13] sc1
	s_add_i32 s3, s3, 1
	s_mov_b64 s[22:23], -1
	s_waitcnt vmcnt(0)
	v_cmp_ge_u32_e32 vcc, v1, v4
	s_orn2_b64 s[26:27], vcc, exec
	s_branch .LBB0_107

; __device__ __forceinline__ unsigned xb_add(unsigned* p, unsigned v) { return __hip_atomic_fetch_add(p, v, __ATOMIC_RELAXED, __HIP_MEMORY_SCOPE_AGENT); }
; __device__ __forceinline__ void xcd_barrier(const XcdBarrier& b, const bool xb_leader) {
;     ...
;             __builtin_amdgcn_fence(__ATOMIC_ACQUIRE, "agent");
;             xb_add(&bar[XB_XGEN(b.x)], 1u);
;             asm volatile("s_waitcnt vmcnt(0)" ::: "memory");
.LBB0_118:
	s_or_b64 exec, exec, s[6:7]
	s_mov_b64 s[6:7], exec
	v_mbcnt_lo_u32_b32 v0, s6, 0
	v_mbcnt_hi_u32_b32 v0, s7, v0
	v_cmp_eq_u32_e32 vcc, 0, v0
	s_waitcnt vmcnt(0)
	s_and_saveexec_b64 s[12:13], vcc
	s_cbranch_execz .LBB0_120
	s_bcnt1_i32_b64 s3, s[6:7]
	v_mov_b32_e32 v0, 0x2000
	v_mov_b32_e32 v1, s3
.LBB0_120:
	s_or_b64 exec, exec, s[12:13]
	s_waitcnt vmcnt(0)

; __device__ __forceinline__ unsigned xb_ld(unsigned* p)              { return __hip_atomic_load(p, __ATOMIC_RELAXED, __HIP_MEMORY_SCOPE_AGENT); }
; __device__ __forceinline__ unsigned xb_add(unsigned* p, unsigned v) { return __hip_atomic_fetch_add(p, v, __ATOMIC_RELAXED, __HIP_MEMORY_SCOPE_AGENT); }
; #define XB_SPIN(cond, bar) do { unsigned _sp = 0; while (cond) { __builtin_amdgcn_s_sleep(1); \
;     if ((++_sp & 255u) == 0u) { if (xb_ld(&(bar)[XB_TMO])) break; if (_sp > XB_SPIN_CAP) { atomicAdd(&(bar)[XB_TMO], 1u); break; } } } } while (0)
; __device__ __forceinline__ void xcd_barrier(const XcdBarrier& b, const bool xb_leader) {
;     ...
;         const unsigned old = xb_add(&bar[XB_XSUB(b.x)], 1u);
;         const unsigned gen = old / nloc;
;         if (old + 1u == (gen + 1u) * nloc) {
;             __builtin_amdgcn_fence(__ATOMIC_RELEASE, "agent");
;             asm volatile("s_waitcnt vmcnt(0)" ::: "memory");
;             const unsigned og = xb_add(&bar[XB_TOP], 1u);
;             const unsigned tg = og / nx;
;             if (og + 1u == (tg + 1u) * nx) xb_add(&bar[XB_TOPGEN], 1u);
;             else XB_SPIN(xb_ld(&bar[XB_TOPGEN]) == tg, bar);
;             __builtin_amdgcn_fence(__ATOMIC_ACQUIRE, "agent");
;             xb_add(&bar[XB_XGEN(b.x)], 1u);
;             asm volatile("s_waitcnt vmcnt(0)" ::: "memory");
;         } else {
;             XB_SPIN(xb_ld(&bar[XB_XGEN(b.x)]) == gen, bar);
.LBB0_180:
	s_or_b64 exec, exec, s[10:11]
	v_cvt_f32_u32_e32 v2, v9
	s_waitcnt vmcnt(0)
	v_readfirstlane_b32 s3, v1
	v_sub_u32_e32 v1, 0, v9
	v_rcp_iflag_f32_e32 v2, v2
	v_add_u32_e32 v3, s3, v0
	v_mul_f32_e32 v2, 0x4f7ffffe, v2
	v_cvt_u32_f32_e32 v2, v2
	v_mul_lo_u32 v0, v1, v2
	v_mul_hi_u32 v0, v2, v0
	v_add_u32_e32 v0, v2, v0
	v_mul_hi_u32 v0, v3, v0
	v_mul_lo_u32 v1, v0, v9
	v_sub_u32_e32 v1, v3, v1
	v_add_u32_e32 v2, 1, v0
	v_cmp_ge_u32_e32 vcc, v1, v9
	s_nop 1
	v_cndmask_b32_e32 v0, v0, v2, vcc
	v_sub_u32_e32 v2, v1, v9
	v_cndmask_b32_e32 v1, v1, v2, vcc
	v_add_u32_e32 v2, 1, v0
	v_cmp_ge_u32_e32 vcc, v1, v9
	v_add_u32_e32 v1, 1, v3
	s_nop 0
	v_cndmask_b32_e32 v0, v0, v2, vcc
	v_mul_lo_u32 v2, v9, v0
	v_add_u32_e32 v2, v2, v9
	v_cmp_ne_u32_e32 vcc, v1, v2
	s_and_saveexec_b64 s[8:9], vcc
	s_xor_b64 s[8:9], exec, s[8:9]
	s_cbranch_execz .LBB0_194
	s_waitcnt lgkmcnt(0)
	v_add_u32_e32 v0, 1, v0
	v_mul_lo_u32 v0, v0, v8
	v_mov_b32_e32 v1, 0x3000
	global_load_dword v1, v1, s[28:29] offset:1024 sc1
	s_add_u32 s12, s28, 0x3400
	s_addc_u32 s13, s29, 0
	s_waitcnt vmcnt(0)
	v_cmp_lt_u32_e32 vcc, v1, v0
	s_and_saveexec_b64 s[10:11], vcc
	s_cbranch_execz .LBB0_193
	s_mov_b32 s3, 1
	s_mov_b64 s[14:15], 0
	v_mov_b32_e32 v1, 0
	s_branch .LBB0_184

; __device__ __forceinline__ unsigned xb_ld(unsigned* p)              { return __hip_atomic_load(p, __ATOMIC_RELAXED, __HIP_MEMORY_SCOPE_AGENT); }
; #define XB_SPIN(cond, bar) do { unsigned _sp = 0; while (cond) { __builtin_amdgcn_s_sleep(1); \
;     if ((++_sp & 255u) == 0u) { if (xb_ld(&(bar)[XB_TMO])) break; if (_sp > XB_SPIN_CAP) { atomicAdd(&(bar)[XB_TMO], 1u); break; } } } } while (0)
; __device__ __forceinline__ void xcd_barrier(const XcdBarrier& b, const bool xb_leader) {
;     ...
;             XB_SPIN(xb_ld(&bar[XB_XGEN(b.x)]) == gen, bar);
.LBB0_188:
	global_load_dword v2, v1, s[12:13] sc1
	s_add_i32 s3, s3, 1
	s_mov_b64 s[20:21], -1
	s_waitcnt vmcnt(0)
	v_cmp_ge_u32_e32 vcc, v2, v0
	s_orn2_b64 s[18:19], vcc, exec
	s_branch .LBB0_183

; __device__ __forceinline__ unsigned xb_ld(unsigned* p)              { return __hip_atomic_load(p, __ATOMIC_RELAXED, __HIP_MEMORY_SCOPE_AGENT); }
; __device__ __forceinline__ unsigned xb_add(unsigned* p, unsigned v) { return __hip_atomic_fetch_add(p, v, __ATOMIC_RELAXED, __HIP_MEMORY_SCOPE_AGENT); }
; #define XB_SPIN(cond, bar) do { unsigned _sp = 0; while (cond) { __builtin_amdgcn_s_sleep(1); \
;     if ((++_sp & 255u) == 0u) { if (xb_ld(&(bar)[XB_TMO])) break; if (_sp > XB_SPIN_CAP) { atomicAdd(&(bar)[XB_TMO], 1u); break; } } } } while (0)
; __device__ __forceinline__ void xcd_barrier(const XcdBarrier& b, const bool xb_leader) {
;     ...
;             const unsigned og = xb_add(&bar[XB_TOP], 1u);
;             const unsigned tg = og / nx;
;             if (og + 1u == (tg + 1u) * nx) xb_add(&bar[XB_TOPGEN], 1u);
;             else XB_SPIN(xb_ld(&bar[XB_TOPGEN]) == tg, bar);
.LBB0_197:
	s_or_b64 exec, exec, s[10:11]
	v_cvt_f32_u32_e32 v2, v8
	s_waitcnt vmcnt(0)
	v_readfirstlane_b32 s3, v1
	s_add_u32 s10, s28, 0x3400
	s_addc_u32 s11, s29, 0
	v_rcp_iflag_f32_e32 v2, v2
	v_add_u32_e32 v0, s3, v0
	v_add_u32_e32 v3, 1, v0
	s_mov_b64 s[12:13], 0
	v_mul_f32_e32 v1, 0x4f7ffffe, v2
	v_cvt_u32_f32_e32 v1, v1
	v_sub_u32_e32 v2, 0, v8
	v_mul_lo_u32 v2, v2, v1
	v_mul_hi_u32 v2, v1, v2
	v_add_u32_e32 v1, v1, v2
	v_mul_hi_u32 v1, v0, v1
	v_mul_lo_u32 v2, v1, v8
	v_sub_u32_e32 v0, v0, v2
	v_add_u32_e32 v4, 1, v1
	v_cmp_ge_u32_e32 vcc, v0, v8
	v_sub_u32_e32 v2, v0, v8
	s_nop 0
	v_cndmask_b32_e32 v1, v1, v4, vcc
	v_cndmask_b32_e32 v0, v0, v2, vcc
	v_add_u32_e32 v2, 1, v1
	v_cmp_ge_u32_e32 vcc, v0, v8
	s_nop 1
	v_cndmask_b32_e32 v2, v1, v2, vcc
	v_mul_lo_u32 v0, v8, v2
	v_add_u32_e32 v0, v0, v8
	v_cmp_ne_u32_e32 vcc, v3, v0
	v_mov_b32_e32 v4, v0
	v_mov_b64_e32 v[0:1], s[10:11]
	s_and_saveexec_b64 s[8:9], vcc
	s_cbranch_execz .LBB0_209
	v_mov_b32_e32 v0, 0
	global_load_dword v1, v0, s[10:11] sc1
	s_mov_b64 s[16:17], 0
	s_waitcnt vmcnt(0)
	v_cmp_lt_u32_e32 vcc, v1, v4
	s_and_saveexec_b64 s[14:15], vcc
	s_cbranch_execz .LBB0_208
	s_add_u32 s12, s28, 0x200
	s_addc_u32 s13, s29, 0
	s_mov_b32 s3, 1
	s_branch .LBB0_201

; __device__ __forceinline__ unsigned xb_ld(unsigned* p)              { return __hip_atomic_load(p, __ATOMIC_RELAXED, __HIP_MEMORY_SCOPE_AGENT); }
; #define XB_SPIN(cond, bar) do { unsigned _sp = 0; while (cond) { __builtin_amdgcn_s_sleep(1); \
;     if ((++_sp & 255u) == 0u) { if (xb_ld(&(bar)[XB_TMO])) break; if (_sp > XB_SPIN_CAP) { atomicAdd(&(bar)[XB_TMO], 1u); break; } } } } while (0)
; __device__ __forceinline__ void xcd_barrier(const XcdBarrier& b, const bool xb_leader) {
;     ...
;             else XB_SPIN(xb_ld(&bar[XB_TOPGEN]) == tg, bar);
.LBB0_205:
	global_load_dword v1, v0, s[10:11] sc1
	s_add_i32 s3, s3, 1
	s_mov_b64 s[20:21], -1
	s_waitcnt vmcnt(0)
	v_cmp_ge_u32_e32 vcc, v1, v4
	s_orn2_b64 s[24:25], vcc, exec
	s_branch .LBB0_200

; __device__ __forceinline__ unsigned xb_add(unsigned* p, unsigned v) { return __hip_atomic_fetch_add(p, v, __ATOMIC_RELAXED, __HIP_MEMORY_SCOPE_AGENT); }
; __device__ __forceinline__ void xcd_barrier(const XcdBarrier& b, const bool xb_leader) {
;     ...
;             __builtin_amdgcn_fence(__ATOMIC_ACQUIRE, "agent");
;             xb_add(&bar[XB_XGEN(b.x)], 1u);
;             asm volatile("s_waitcnt vmcnt(0)" ::: "memory");
.LBB0_211:
	s_or_b64 exec, exec, s[8:9]
	s_mov_b64 s[8:9], exec
	v_mbcnt_lo_u32_b32 v0, s8, 0
	v_mbcnt_hi_u32_b32 v0, s9, v0
	v_cmp_eq_u32_e32 vcc, 0, v0
	s_waitcnt vmcnt(0)
	s_and_saveexec_b64 s[10:11], vcc
	s_cbranch_execz .LBB0_213
	s_bcnt1_i32_b64 s3, s[8:9]
	v_mov_b32_e32 v0, 0x2000
	v_mov_b32_e32 v1, s3
.LBB0_213:
	s_or_b64 exec, exec, s[10:11]
	s_waitcnt vmcnt(0)

; __device__ __forceinline__ unsigned xb_add(unsigned* p, unsigned v) { return __hip_atomic_fetch_add(p, v, __ATOMIC_RELAXED, __HIP_MEMORY_SCOPE_AGENT); }
; __device__ __forceinline__ void xcd_barrier(const XcdBarrier& b, const bool xb_leader) {
;     ...
;             __builtin_amdgcn_fence(__ATOMIC_ACQUIRE, "agent");
;             xb_add(&bar[XB_XGEN(b.x)], 1u);
;             asm volatile("s_waitcnt vmcnt(0)" ::: "memory");
.LBB0_367:
	s_or_b64 exec, exec, s[8:9]
	s_mov_b64 s[8:9], exec
	v_mbcnt_lo_u32_b32 v0, s8, 0
	v_mbcnt_hi_u32_b32 v0, s9, v0
	v_cmp_eq_u32_e32 vcc, 0, v0
	s_waitcnt vmcnt(0)
	s_and_saveexec_b64 s[10:11], vcc
	s_cbranch_execz .LBB0_369
	s_bcnt1_i32_b64 s3, s[8:9]
	v_mov_b32_e32 v0, 0x2000
	v_mov_b32_e32 v1, s3
.LBB0_369:
	s_or_b64 exec, exec, s[10:11]
	s_waitcnt vmcnt(0)

; __device__ __forceinline__ unsigned xb_add(unsigned* p, unsigned v) { return __hip_atomic_fetch_add(p, v, __ATOMIC_RELAXED, __HIP_MEMORY_SCOPE_AGENT); }
; __device__ __forceinline__ void xcd_barrier(const XcdBarrier& b, const bool xb_leader) {
;     ...
;             __builtin_amdgcn_fence(__ATOMIC_ACQUIRE, "agent");
;             xb_add(&bar[XB_XGEN(b.x)], 1u);
;             asm volatile("s_waitcnt vmcnt(0)" ::: "memory");
.LBB0_643:
	s_or_b64 exec, exec, s[8:9]
	s_mov_b64 s[8:9], exec
	v_mbcnt_lo_u32_b32 v0, s8, 0
	v_mbcnt_hi_u32_b32 v0, s9, v0
	v_cmp_eq_u32_e32 vcc, 0, v0
	s_waitcnt vmcnt(0)
	s_and_saveexec_b64 s[10:11], vcc
	s_cbranch_execz .LBB0_645
	s_bcnt1_i32_b64 s3, s[8:9]
	v_mov_b32_e32 v0, 0x2000
	v_mov_b32_e32 v1, s3
.LBB0_645:
	s_or_b64 exec, exec, s[10:11]
	s_waitcnt vmcnt(0)

; __device__ __forceinline__ unsigned xb_ld(unsigned* p)              { return __hip_atomic_load(p, __ATOMIC_RELAXED, __HIP_MEMORY_SCOPE_AGENT); }
; __device__ __forceinline__ unsigned xb_add(unsigned* p, unsigned v) { return __hip_atomic_fetch_add(p, v, __ATOMIC_RELAXED, __HIP_MEMORY_SCOPE_AGENT); }
; #define XB_SPIN(cond, bar) do { unsigned _sp = 0; while (cond) { __builtin_amdgcn_s_sleep(1); \
;     if ((++_sp & 255u) == 0u) { if (xb_ld(&(bar)[XB_TMO])) break; if (_sp > XB_SPIN_CAP) { atomicAdd(&(bar)[XB_TMO], 1u); break; } } } } while (0)
; __device__ __forceinline__ void xcd_barrier(const XcdBarrier& b, const bool xb_leader) {
;     ...
;         const unsigned old = xb_add(&bar[XB_XSUB(b.x)], 1u);
;         const unsigned gen = old / nloc;
;         if (old + 1u == (gen + 1u) * nloc) {
;             __builtin_amdgcn_fence(__ATOMIC_RELEASE, "agent");
;             asm volatile("s_waitcnt vmcnt(0)" ::: "memory");
;             const unsigned og = xb_add(&bar[XB_TOP], 1u);
;             const unsigned tg = og / nx;
;             if (og + 1u == (tg + 1u) * nx) xb_add(&bar[XB_TOPGEN], 1u);
;             else XB_SPIN(xb_ld(&bar[XB_TOPGEN]) == tg, bar);
;             __builtin_amdgcn_fence(__ATOMIC_ACQUIRE, "agent");
;             xb_add(&bar[XB_XGEN(b.x)], 1u);
;             asm volatile("s_waitcnt vmcnt(0)" ::: "memory");
;         } else {
;             XB_SPIN(xb_ld(&bar[XB_XGEN(b.x)]) == gen, bar);
.LBB0_821:
	s_or_b64 exec, exec, s[8:9]
	v_cvt_f32_u32_e32 v2, v9
	s_waitcnt vmcnt(0)
	v_readfirstlane_b32 s3, v1
	v_sub_u32_e32 v1, 0, v9
	v_rcp_iflag_f32_e32 v2, v2
	v_add_u32_e32 v3, s3, v0
	v_mul_f32_e32 v2, 0x4f7ffffe, v2
	v_cvt_u32_f32_e32 v2, v2
	v_mul_lo_u32 v0, v1, v2
	v_mul_hi_u32 v0, v2, v0
	v_add_u32_e32 v0, v2, v0
	v_mul_hi_u32 v0, v3, v0
	v_mul_lo_u32 v1, v0, v9
	v_sub_u32_e32 v1, v3, v1
	v_add_u32_e32 v2, 1, v0
	v_cmp_ge_u32_e32 vcc, v1, v9
	s_nop 1
	v_cndmask_b32_e32 v0, v0, v2, vcc
	v_sub_u32_e32 v2, v1, v9
	v_cndmask_b32_e32 v1, v1, v2, vcc
	v_add_u32_e32 v2, 1, v0
	v_cmp_ge_u32_e32 vcc, v1, v9
	v_add_u32_e32 v1, 1, v3
	s_nop 0
	v_cndmask_b32_e32 v0, v0, v2, vcc
	v_mul_lo_u32 v2, v9, v0
	v_add_u32_e32 v2, v2, v9
	v_cmp_ne_u32_e32 vcc, v1, v2
	s_and_saveexec_b64 s[6:7], vcc
	s_xor_b64 s[6:7], exec, s[6:7]
	s_cbranch_execz .LBB0_835
	s_waitcnt lgkmcnt(0)
	v_add_u32_e32 v0, 1, v0
	v_mul_lo_u32 v0, v0, v8
	v_mov_b32_e32 v1, 0x3000
	global_load_dword v1, v1, s[28:29] offset:1024 sc1
	s_add_u32 s10, s28, 0x3400
	s_addc_u32 s11, s29, 0
	s_waitcnt vmcnt(0)
	v_cmp_lt_u32_e32 vcc, v1, v0
	s_and_saveexec_b64 s[8:9], vcc
	s_cbranch_execz .LBB0_834
	s_mov_b32 s3, 1
	s_mov_b64 s[12:13], 0
	v_mov_b32_e32 v1, 0
	s_branch .LBB0_825

; __device__ __forceinline__ unsigned xb_ld(unsigned* p)              { return __hip_atomic_load(p, __ATOMIC_RELAXED, __HIP_MEMORY_SCOPE_AGENT); }
; __device__ __forceinline__ unsigned xb_add(unsigned* p, unsigned v) { return __hip_atomic_fetch_add(p, v, __ATOMIC_RELAXED, __HIP_MEMORY_SCOPE_AGENT); }
; #define XB_SPIN(cond, bar) do { unsigned _sp = 0; while (cond) { __builtin_amdgcn_s_sleep(1); \
;     if ((++_sp & 255u) == 0u) { if (xb_ld(&(bar)[XB_TMO])) break; if (_sp > XB_SPIN_CAP) { atomicAdd(&(bar)[XB_TMO], 1u); break; } } } } while (0)
; __device__ __forceinline__ void xcd_barrier(const XcdBarrier& b, const bool xb_leader) {
;     ...
;             else XB_SPIN(xb_ld(&bar[XB_TOPGEN]) == tg, bar);
;             __builtin_amdgcn_fence(__ATOMIC_ACQUIRE, "agent");
;             xb_add(&bar[XB_XGEN(b.x)], 1u);
;             asm volatile("s_waitcnt vmcnt(0)" ::: "memory");
;         } else {
;             XB_SPIN(xb_ld(&bar[XB_XGEN(b.x)]) == gen, bar);
.LBB0_829:
	global_load_dword v2, v1, s[10:11] sc1
	s_add_i32 s3, s3, 1
	s_mov_b64 s[20:21], -1
	s_waitcnt vmcnt(0)
	v_cmp_ge_u32_e32 vcc, v2, v0
	s_orn2_b64 s[16:17], vcc, exec
	s_branch .LBB0_824

; __device__ __forceinline__ unsigned xb_ld(unsigned* p)              { return __hip_atomic_load(p, __ATOMIC_RELAXED, __HIP_MEMORY_SCOPE_AGENT); }
; __device__ __forceinline__ unsigned xb_add(unsigned* p, unsigned v) { return __hip_atomic_fetch_add(p, v, __ATOMIC_RELAXED, __HIP_MEMORY_SCOPE_AGENT); }
; #define XB_SPIN(cond, bar) do { unsigned _sp = 0; while (cond) { __builtin_amdgcn_s_sleep(1); \
;     if ((++_sp & 255u) == 0u) { if (xb_ld(&(bar)[XB_TMO])) break; if (_sp > XB_SPIN_CAP) { atomicAdd(&(bar)[XB_TMO], 1u); break; } } } } while (0)
; __device__ __forceinline__ void xcd_barrier(const XcdBarrier& b, const bool xb_leader) {
;     ...
;         const unsigned old = xb_add(&bar[XB_XSUB(b.x)], 1u);
;         const unsigned gen = old / nloc;
;         if (old + 1u == (gen + 1u) * nloc) {
;             __builtin_amdgcn_fence(__ATOMIC_RELEASE, "agent");
;             asm volatile("s_waitcnt vmcnt(0)" ::: "memory");
;             const unsigned og = xb_add(&bar[XB_TOP], 1u);
;             const unsigned tg = og / nx;
;             if (og + 1u == (tg + 1u) * nx) xb_add(&bar[XB_TOPGEN], 1u);
;             else XB_SPIN(xb_ld(&bar[XB_TOPGEN]) == tg, bar);
.LBB0_838:
	s_or_b64 exec, exec, s[8:9]
	v_cvt_f32_u32_e32 v2, v8
	s_waitcnt vmcnt(0)
	v_readfirstlane_b32 s3, v1
	s_add_u32 s8, s28, 0x3400
	s_addc_u32 s9, s29, 0
	v_rcp_iflag_f32_e32 v2, v2
	v_add_u32_e32 v0, s3, v0
	v_add_u32_e32 v3, 1, v0
	s_mov_b64 s[10:11], 0
	v_mul_f32_e32 v1, 0x4f7ffffe, v2
	v_cvt_u32_f32_e32 v1, v1
	v_sub_u32_e32 v2, 0, v8
	v_mul_lo_u32 v2, v2, v1
	v_mul_hi_u32 v2, v1, v2
	v_add_u32_e32 v1, v1, v2
	v_mul_hi_u32 v1, v0, v1
	v_mul_lo_u32 v2, v1, v8
	v_sub_u32_e32 v0, v0, v2
	v_add_u32_e32 v4, 1, v1
	v_cmp_ge_u32_e32 vcc, v0, v8
	v_sub_u32_e32 v2, v0, v8
	s_nop 0
	v_cndmask_b32_e32 v1, v1, v4, vcc
	v_cndmask_b32_e32 v0, v0, v2, vcc
	v_add_u32_e32 v2, 1, v1
	v_cmp_ge_u32_e32 vcc, v0, v8
	s_nop 1
	v_cndmask_b32_e32 v2, v1, v2, vcc
	v_mul_lo_u32 v0, v8, v2
	v_add_u32_e32 v0, v0, v8
	v_cmp_ne_u32_e32 vcc, v3, v0
	v_mov_b32_e32 v4, v0
	v_mov_b64_e32 v[0:1], s[8:9]
	s_and_saveexec_b64 s[6:7], vcc
	s_cbranch_execz .LBB0_850
	v_mov_b32_e32 v0, 0
	global_load_dword v1, v0, s[8:9] sc1
	s_mov_b64 s[14:15], 0
	s_waitcnt vmcnt(0)
	v_cmp_lt_u32_e32 vcc, v1, v4
	s_and_saveexec_b64 s[12:13], vcc
	s_cbranch_execz .LBB0_849
	s_add_u32 s10, s28, 0x200
	s_addc_u32 s11, s29, 0
	s_mov_b32 s3, 1
	s_branch .LBB0_842

; __device__ __forceinline__ unsigned xb_ld(unsigned* p)              { return __hip_atomic_load(p, __ATOMIC_RELAXED, __HIP_MEMORY_SCOPE_AGENT); }
; #define XB_SPIN(cond, bar) do { unsigned _sp = 0; while (cond) { __builtin_amdgcn_s_sleep(1); \
;     if ((++_sp & 255u) == 0u) { if (xb_ld(&(bar)[XB_TMO])) break; if (_sp > XB_SPIN_CAP) { atomicAdd(&(bar)[XB_TMO], 1u); break; } } } } while (0)
; __device__ __forceinline__ void xcd_barrier(const XcdBarrier& b, const bool xb_leader) {
;     ...
;             else XB_SPIN(xb_ld(&bar[XB_TOPGEN]) == tg, bar);
.LBB0_846:
	global_load_dword v1, v0, s[8:9] sc1
	s_add_i32 s3, s3, 1
	s_mov_b64 s[20:21], -1
	s_waitcnt vmcnt(0)
	v_cmp_ge_u32_e32 vcc, v1, v4
	s_orn2_b64 s[24:25], vcc, exec
	s_branch .LBB0_841

; __device__ __forceinline__ unsigned xb_add(unsigned* p, unsigned v) { return __hip_atomic_fetch_add(p, v, __ATOMIC_RELAXED, __HIP_MEMORY_SCOPE_AGENT); }
; __device__ __forceinline__ void xcd_barrier(const XcdBarrier& b, const bool xb_leader) {
;     ...
;             __builtin_amdgcn_fence(__ATOMIC_ACQUIRE, "agent");
;             xb_add(&bar[XB_XGEN(b.x)], 1u);
;             asm volatile("s_waitcnt vmcnt(0)" ::: "memory");
.LBB0_852:
	s_or_b64 exec, exec, s[6:7]
	s_mov_b64 s[6:7], exec
	v_mbcnt_lo_u32_b32 v0, s6, 0
	v_mbcnt_hi_u32_b32 v0, s7, v0
	v_cmp_eq_u32_e32 vcc, 0, v0
	s_waitcnt vmcnt(0)
	s_and_saveexec_b64 s[8:9], vcc
	s_cbranch_execz .LBB0_854
	s_bcnt1_i32_b64 s3, s[6:7]
	v_mov_b32_e32 v0, 0x2000
	v_mov_b32_e32 v1, s3
.LBB0_854:
	s_or_b64 exec, exec, s[8:9]
	s_waitcnt vmcnt(0)

; __device__ __forceinline__ unsigned xb_ld(unsigned* p)              { return __hip_atomic_load(p, __ATOMIC_RELAXED, __HIP_MEMORY_SCOPE_AGENT); }
; __device__ __forceinline__ unsigned xb_add(unsigned* p, unsigned v) { return __hip_atomic_fetch_add(p, v, __ATOMIC_RELAXED, __HIP_MEMORY_SCOPE_AGENT); }
; #define XB_SPIN(cond, bar) do { unsigned _sp = 0; while (cond) { __builtin_amdgcn_s_sleep(1); \
;     if ((++_sp & 255u) == 0u) { if (xb_ld(&(bar)[XB_TMO])) break; if (_sp > XB_SPIN_CAP) { atomicAdd(&(bar)[XB_TMO], 1u); break; } } } } while (0)
; __device__ __forceinline__ void xcd_barrier(const XcdBarrier& b, const bool xb_leader) {
;     ...
;             else XB_SPIN(xb_ld(&bar[XB_TOPGEN]) == tg, bar);
;             __builtin_amdgcn_fence(__ATOMIC_ACQUIRE, "agent");
;             xb_add(&bar[XB_XGEN(b.x)], 1u);
;             asm volatile("s_waitcnt vmcnt(0)" ::: "memory");
;         } else {
;             XB_SPIN(xb_ld(&bar[XB_XGEN(b.x)]) == gen, bar);
.LBB0_932:
	global_load_dword v2, v1, s[12:13] sc1
	s_add_i32 s3, s3, 1
	s_mov_b64 s[24:25], -1
	s_waitcnt vmcnt(0)
	v_cmp_ge_u32_e32 vcc, v2, v0
	s_orn2_b64 s[22:23], vcc, exec
	s_branch .LBB0_927

; __device__ __forceinline__ unsigned xb_ld(unsigned* p)              { return __hip_atomic_load(p, __ATOMIC_RELAXED, __HIP_MEMORY_SCOPE_AGENT); }
; #define XB_SPIN(cond, bar) do { unsigned _sp = 0; while (cond) { __builtin_amdgcn_s_sleep(1); \
;     if ((++_sp & 255u) == 0u) { if (xb_ld(&(bar)[XB_TMO])) break; if (_sp > XB_SPIN_CAP) { atomicAdd(&(bar)[XB_TMO], 1u); break; } } } } while (0)
; __device__ __forceinline__ void xcd_barrier(const XcdBarrier& b, const bool xb_leader) {
;     ...
;             else XB_SPIN(xb_ld(&bar[XB_TOPGEN]) == tg, bar);
.LBB0_949:
	global_load_dword v1, v0, s[10:11] sc1
	s_add_i32 s3, s3, 1
	s_mov_b64 s[24:25], -1
	s_waitcnt vmcnt(0)
	v_cmp_ge_u32_e32 vcc, v1, v4
	s_orn2_b64 s[30:31], vcc, exec
	s_branch .LBB0_944

; __device__ __forceinline__ unsigned xb_add(unsigned* p, unsigned v) { return __hip_atomic_fetch_add(p, v, __ATOMIC_RELAXED, __HIP_MEMORY_SCOPE_AGENT); }
; __device__ __forceinline__ void xcd_barrier(const XcdBarrier& b, const bool xb_leader) {
;     ...
;             __builtin_amdgcn_fence(__ATOMIC_ACQUIRE, "agent");
;             xb_add(&bar[XB_XGEN(b.x)], 1u);
;             asm volatile("s_waitcnt vmcnt(0)" ::: "memory");
.LBB0_955:
	s_or_b64 exec, exec, s[8:9]
	s_mov_b64 s[8:9], exec
	v_mbcnt_lo_u32_b32 v0, s8, 0
	v_mbcnt_hi_u32_b32 v0, s9, v0
	v_cmp_eq_u32_e32 vcc, 0, v0
	s_waitcnt vmcnt(0)
	s_and_saveexec_b64 s[10:11], vcc
	s_cbranch_execz .LBB0_957
	s_bcnt1_i32_b64 s3, s[8:9]
	v_mov_b32_e32 v0, 0x2000
	v_mov_b32_e32 v1, s3
.LBB0_957:
	s_or_b64 exec, exec, s[10:11]
	s_waitcnt vmcnt(0)

; __device__ __forceinline__ unsigned xb_ld(unsigned* p)              { return __hip_atomic_load(p, __ATOMIC_RELAXED, __HIP_MEMORY_SCOPE_AGENT); }
; __device__ __forceinline__ unsigned xb_add(unsigned* p, unsigned v) { return __hip_atomic_fetch_add(p, v, __ATOMIC_RELAXED, __HIP_MEMORY_SCOPE_AGENT); }
; #define XB_SPIN(cond, bar) do { unsigned _sp = 0; while (cond) { __builtin_amdgcn_s_sleep(1); \
;     if ((++_sp & 255u) == 0u) { if (xb_ld(&(bar)[XB_TMO])) break; if (_sp > XB_SPIN_CAP) { atomicAdd(&(bar)[XB_TMO], 1u); break; } } } } while (0)
; __device__ __forceinline__ void xcd_barrier(const XcdBarrier& b, const bool xb_leader) {
;     ...
;             else XB_SPIN(xb_ld(&bar[XB_TOPGEN]) == tg, bar);
;             __builtin_amdgcn_fence(__ATOMIC_ACQUIRE, "agent");
;             xb_add(&bar[XB_XGEN(b.x)], 1u);
;             asm volatile("s_waitcnt vmcnt(0)" ::: "memory");
;         } else {
;             XB_SPIN(xb_ld(&bar[XB_XGEN(b.x)]) == gen, bar);
.LBB0_1082:
	global_load_dword v2, v1, s[10:11] sc1
	s_add_i32 s3, s3, 1
	s_mov_b64 s[24:25], -1
	s_waitcnt vmcnt(0)
	v_cmp_ge_u32_e32 vcc, v2, v0
	s_orn2_b64 s[16:17], vcc, exec
	s_branch .LBB0_1077

; __device__ __forceinline__ unsigned xb_ld(unsigned* p)              { return __hip_atomic_load(p, __ATOMIC_RELAXED, __HIP_MEMORY_SCOPE_AGENT); }
; #define XB_SPIN(cond, bar) do { unsigned _sp = 0; while (cond) { __builtin_amdgcn_s_sleep(1); \
;     if ((++_sp & 255u) == 0u) { if (xb_ld(&(bar)[XB_TMO])) break; if (_sp > XB_SPIN_CAP) { atomicAdd(&(bar)[XB_TMO], 1u); break; } } } } while (0)
; __device__ __forceinline__ void xcd_barrier(const XcdBarrier& b, const bool xb_leader) {
;     ...
;             else XB_SPIN(xb_ld(&bar[XB_TOPGEN]) == tg, bar);
.LBB0_1099:
	global_load_dword v1, v0, s[8:9] sc1
	s_add_i32 s3, s3, 1
	s_mov_b64 s[24:25], -1
	s_waitcnt vmcnt(0)
	v_cmp_ge_u32_e32 vcc, v1, v4
	s_orn2_b64 s[30:31], vcc, exec
	s_branch .LBB0_1094

; __device__ __forceinline__ unsigned xb_add(unsigned* p, unsigned v) { return __hip_atomic_fetch_add(p, v, __ATOMIC_RELAXED, __HIP_MEMORY_SCOPE_AGENT); }
; __device__ __forceinline__ void xcd_barrier(const XcdBarrier& b, const bool xb_leader) {
;     ...
;             __builtin_amdgcn_fence(__ATOMIC_ACQUIRE, "agent");
;             xb_add(&bar[XB_XGEN(b.x)], 1u);
;             asm volatile("s_waitcnt vmcnt(0)" ::: "memory");
.LBB0_1105:
	s_or_b64 exec, exec, s[6:7]
	s_mov_b64 s[6:7], exec
	v_mbcnt_lo_u32_b32 v0, s6, 0
	v_mbcnt_hi_u32_b32 v0, s7, v0
	v_cmp_eq_u32_e32 vcc, 0, v0
	s_waitcnt vmcnt(0)
	s_and_saveexec_b64 s[8:9], vcc
	s_cbranch_execz .LBB0_1107
	s_bcnt1_i32_b64 s3, s[6:7]
	v_mov_b32_e32 v0, 0x2000
	v_mov_b32_e32 v1, s3
.LBB0_1107:
	s_or_b64 exec, exec, s[8:9]
	s_waitcnt vmcnt(0)

; __device__ __forceinline__ unsigned xb_ld(unsigned* p)              { return __hip_atomic_load(p, __ATOMIC_RELAXED, __HIP_MEMORY_SCOPE_AGENT); }
; __device__ __forceinline__ unsigned xb_add(unsigned* p, unsigned v) { return __hip_atomic_fetch_add(p, v, __ATOMIC_RELAXED, __HIP_MEMORY_SCOPE_AGENT); }
; #define XB_SPIN(cond, bar) do { unsigned _sp = 0; while (cond) { __builtin_amdgcn_s_sleep(1); \
;     if ((++_sp & 255u) == 0u) { if (xb_ld(&(bar)[XB_TMO])) break; if (_sp > XB_SPIN_CAP) { atomicAdd(&(bar)[XB_TMO], 1u); break; } } } } while (0)
; __device__ __forceinline__ void xcd_barrier(const XcdBarrier& b, const bool xb_leader) {
;     ...
;             else XB_SPIN(xb_ld(&bar[XB_TOPGEN]) == tg, bar);
;             __builtin_amdgcn_fence(__ATOMIC_ACQUIRE, "agent");
;             xb_add(&bar[XB_XGEN(b.x)], 1u);
;             asm volatile("s_waitcnt vmcnt(0)" ::: "memory");
;         } else {
;             XB_SPIN(xb_ld(&bar[XB_XGEN(b.x)]) == gen, bar);
.LBB0_1221:
	global_load_dword v2, v1, s[12:13] sc1
	s_add_i32 s3, s3, 1
	s_mov_b64 s[26:27], -1
	s_waitcnt vmcnt(0)
	v_cmp_ge_u32_e32 vcc, v2, v0
	s_orn2_b64 s[24:25], vcc, exec
	s_branch .LBB0_1216

; __device__ __forceinline__ unsigned xb_ld(unsigned* p)              { return __hip_atomic_load(p, __ATOMIC_RELAXED, __HIP_MEMORY_SCOPE_AGENT); }
; #define XB_SPIN(cond, bar) do { unsigned _sp = 0; while (cond) { __builtin_amdgcn_s_sleep(1); \
;     if ((++_sp & 255u) == 0u) { if (xb_ld(&(bar)[XB_TMO])) break; if (_sp > XB_SPIN_CAP) { atomicAdd(&(bar)[XB_TMO], 1u); break; } } } } while (0)
; __device__ __forceinline__ void xcd_barrier(const XcdBarrier& b, const bool xb_leader) {
;     ...
;             else XB_SPIN(xb_ld(&bar[XB_TOPGEN]) == tg, bar);
.LBB0_1238:
	global_load_dword v1, v0, s[10:11] sc1
	s_add_i32 s3, s3, 1
	s_mov_b64 s[26:27], -1
	s_waitcnt vmcnt(0)
	v_cmp_ge_u32_e32 vcc, v1, v4
	s_orn2_b64 s[36:37], vcc, exec
	s_branch .LBB0_1233

; __device__ __forceinline__ unsigned xb_add(unsigned* p, unsigned v) { return __hip_atomic_fetch_add(p, v, __ATOMIC_RELAXED, __HIP_MEMORY_SCOPE_AGENT); }
; __device__ __forceinline__ void xcd_barrier(const XcdBarrier& b, const bool xb_leader) {
;     ...
;             __builtin_amdgcn_fence(__ATOMIC_ACQUIRE, "agent");
;             xb_add(&bar[XB_XGEN(b.x)], 1u);
;             asm volatile("s_waitcnt vmcnt(0)" ::: "memory");
.LBB0_1244:
	s_or_b64 exec, exec, s[8:9]
	s_mov_b64 s[8:9], exec
	v_mbcnt_lo_u32_b32 v0, s8, 0
	v_mbcnt_hi_u32_b32 v0, s9, v0
	v_cmp_eq_u32_e32 vcc, 0, v0
	s_waitcnt vmcnt(0)
	s_and_saveexec_b64 s[10:11], vcc
	s_cbranch_execz .LBB0_1246
	s_bcnt1_i32_b64 s3, s[8:9]
	v_mov_b32_e32 v0, 0x2000
	v_mov_b32_e32 v1, s3
.LBB0_1246:
	s_or_b64 exec, exec, s[10:11]
	s_waitcnt vmcnt(0)

; __device__ __forceinline__ unsigned xb_add(unsigned* p, unsigned v) { return __hip_atomic_fetch_add(p, v, __ATOMIC_RELAXED, __HIP_MEMORY_SCOPE_AGENT); }
; __device__ __forceinline__ void xcd_barrier(const XcdBarrier& b, const bool xb_leader) {
;     ...
;             __builtin_amdgcn_fence(__ATOMIC_ACQUIRE, "agent");
;             xb_add(&bar[XB_XGEN(b.x)], 1u);
;             asm volatile("s_waitcnt vmcnt(0)" ::: "memory");
.LBB0_1516:
	s_or_b64 exec, exec, s[8:9]
	s_mov_b64 s[8:9], exec
	v_mbcnt_lo_u32_b32 v0, s8, 0
	v_mbcnt_hi_u32_b32 v0, s9, v0
	v_cmp_eq_u32_e32 vcc, 0, v0
	s_waitcnt vmcnt(0)
	s_and_saveexec_b64 s[10:11], vcc
	s_cbranch_execz .LBB0_1518
	s_bcnt1_i32_b64 s3, s[8:9]
	v_mov_b32_e32 v0, 0x2000
	v_mov_b32_e32 v1, s3
.LBB0_1518:
	s_or_b64 exec, exec, s[10:11]
	s_waitcnt vmcnt(0)

; __device__ __forceinline__ unsigned xb_ld(unsigned* p)              { return __hip_atomic_load(p, __ATOMIC_RELAXED, __HIP_MEMORY_SCOPE_AGENT); }
; __device__ __forceinline__ unsigned xb_add(unsigned* p, unsigned v) { return __hip_atomic_fetch_add(p, v, __ATOMIC_RELAXED, __HIP_MEMORY_SCOPE_AGENT); }
; #define XB_SPIN(cond, bar) do { unsigned _sp = 0; while (cond) { __builtin_amdgcn_s_sleep(1); \
;     if ((++_sp & 255u) == 0u) { if (xb_ld(&(bar)[XB_TMO])) break; if (_sp > XB_SPIN_CAP) { atomicAdd(&(bar)[XB_TMO], 1u); break; } } } } while (0)
; __device__ __forceinline__ void xcd_barrier(const XcdBarrier& b, const bool xb_leader) {
;     ...
;         const unsigned old = xb_add(&bar[XB_XSUB(b.x)], 1u);
;         const unsigned gen = old / nloc;
;         if (old + 1u == (gen + 1u) * nloc) {
;             __builtin_amdgcn_fence(__ATOMIC_RELEASE, "agent");
;             asm volatile("s_waitcnt vmcnt(0)" ::: "memory");
;             const unsigned og = xb_add(&bar[XB_TOP], 1u);
;             const unsigned tg = og / nx;
;             if (og + 1u == (tg + 1u) * nx) xb_add(&bar[XB_TOPGEN], 1u);
;             else XB_SPIN(xb_ld(&bar[XB_TOPGEN]) == tg, bar);
;             __builtin_amdgcn_fence(__ATOMIC_ACQUIRE, "agent");
;             xb_add(&bar[XB_XGEN(b.x)], 1u);
;             asm volatile("s_waitcnt vmcnt(0)" ::: "memory");
;         } else {
;             XB_SPIN(xb_ld(&bar[XB_XGEN(b.x)]) == gen, bar);
;             __builtin_amdgcn_fence(__ATOMIC_ACQUIRE, "agent");
;             asm volatile("s_waitcnt vmcnt(0)" ::: "memory");
;         }
.LBB0_1592:
	s_or_b64 exec, exec, s[10:11]
	v_cvt_f32_u32_e32 v2, v9
	s_waitcnt vmcnt(0)
	v_readfirstlane_b32 s3, v1
	v_sub_u32_e32 v1, 0, v9
	v_rcp_iflag_f32_e32 v2, v2
	v_add_u32_e32 v3, s3, v0
	v_mul_f32_e32 v2, 0x4f7ffffe, v2
	v_cvt_u32_f32_e32 v2, v2
	v_mul_lo_u32 v0, v1, v2
	v_mul_hi_u32 v0, v2, v0
	v_add_u32_e32 v0, v2, v0
	v_mul_hi_u32 v0, v3, v0
	v_mul_lo_u32 v1, v0, v9
	v_sub_u32_e32 v1, v3, v1
	v_add_u32_e32 v2, 1, v0
	v_cmp_ge_u32_e32 vcc, v1, v9
	s_nop 1
	v_cndmask_b32_e32 v0, v0, v2, vcc
	v_sub_u32_e32 v2, v1, v9
	v_cndmask_b32_e32 v1, v1, v2, vcc
	v_add_u32_e32 v2, 1, v0
	v_cmp_ge_u32_e32 vcc, v1, v9
	v_add_u32_e32 v1, 1, v3
	s_nop 0
	v_cndmask_b32_e32 v0, v0, v2, vcc
	v_mul_lo_u32 v2, v9, v0
	v_add_u32_e32 v2, v2, v9
	v_cmp_ne_u32_e32 vcc, v1, v2
	s_and_saveexec_b64 s[6:7], vcc
	s_xor_b64 s[6:7], exec, s[6:7]
	s_cbranch_execz .LBB0_1606
	s_waitcnt lgkmcnt(0)
	v_add_u32_e32 v0, 1, v0
	v_mul_lo_u32 v0, v0, v8
	v_mov_b32_e32 v1, 0x3000
	global_load_dword v1, v1, s[28:29] offset:1024 sc1
	s_add_u32 s12, s28, 0x3400
	s_addc_u32 s13, s29, 0
	s_waitcnt vmcnt(0)
	v_cmp_lt_u32_e32 vcc, v1, v0
	s_and_saveexec_b64 s[10:11], vcc
	s_cbranch_execz .LBB0_1605
	s_mov_b32 s3, 1
	s_mov_b64 s[14:15], 0
	v_mov_b32_e32 v1, 0
	s_branch .LBB0_1596

; __device__ __forceinline__ unsigned xb_ld(unsigned* p)              { return __hip_atomic_load(p, __ATOMIC_RELAXED, __HIP_MEMORY_SCOPE_AGENT); }
; __device__ __forceinline__ unsigned xb_add(unsigned* p, unsigned v) { return __hip_atomic_fetch_add(p, v, __ATOMIC_RELAXED, __HIP_MEMORY_SCOPE_AGENT); }
; #define XB_SPIN(cond, bar) do { unsigned _sp = 0; while (cond) { __builtin_amdgcn_s_sleep(1); \
;     if ((++_sp & 255u) == 0u) { if (xb_ld(&(bar)[XB_TMO])) break; if (_sp > XB_SPIN_CAP) { atomicAdd(&(bar)[XB_TMO], 1u); break; } } } } while (0)
; __device__ __forceinline__ void xcd_barrier(const XcdBarrier& b, const bool xb_leader) {
;     ...
;         const unsigned old = xb_add(&bar[XB_XSUB(b.x)], 1u);
;         const unsigned gen = old / nloc;
;         if (old + 1u == (gen + 1u) * nloc) {
;             __builtin_amdgcn_fence(__ATOMIC_RELEASE, "agent");
;             asm volatile("s_waitcnt vmcnt(0)" ::: "memory");
;             const unsigned og = xb_add(&bar[XB_TOP], 1u);
;             const unsigned tg = og / nx;
;             if (og + 1u == (tg + 1u) * nx) xb_add(&bar[XB_TOPGEN], 1u);
;             else XB_SPIN(xb_ld(&bar[XB_TOPGEN]) == tg, bar);
.LBB0_1609:
	s_or_b64 exec, exec, s[10:11]
	v_cvt_f32_u32_e32 v2, v8
	s_waitcnt vmcnt(0)
	v_readfirstlane_b32 s3, v1
	s_add_u32 s10, s28, 0x3400
	s_addc_u32 s11, s29, 0
	v_rcp_iflag_f32_e32 v2, v2
	v_add_u32_e32 v0, s3, v0
	v_add_u32_e32 v3, 1, v0
	s_mov_b64 s[12:13], 0
	v_mul_f32_e32 v1, 0x4f7ffffe, v2
	v_cvt_u32_f32_e32 v1, v1
	v_sub_u32_e32 v2, 0, v8
	v_mul_lo_u32 v2, v2, v1
	v_mul_hi_u32 v2, v1, v2
	v_add_u32_e32 v1, v1, v2
	v_mul_hi_u32 v1, v0, v1
	v_mul_lo_u32 v2, v1, v8
	v_sub_u32_e32 v0, v0, v2
	v_add_u32_e32 v4, 1, v1
	v_cmp_ge_u32_e32 vcc, v0, v8
	v_sub_u32_e32 v2, v0, v8
	s_nop 0
	v_cndmask_b32_e32 v1, v1, v4, vcc
	v_cndmask_b32_e32 v0, v0, v2, vcc
	v_add_u32_e32 v2, 1, v1
	v_cmp_ge_u32_e32 vcc, v0, v8
	s_nop 1
	v_cndmask_b32_e32 v2, v1, v2, vcc
	v_mul_lo_u32 v0, v8, v2
	v_add_u32_e32 v0, v0, v8
	v_cmp_ne_u32_e32 vcc, v3, v0
	v_mov_b32_e32 v4, v0
	v_mov_b64_e32 v[0:1], s[10:11]
	s_and_saveexec_b64 s[6:7], vcc
	s_cbranch_execz .LBB0_1621
	v_mov_b32_e32 v0, 0
	global_load_dword v1, v0, s[10:11] sc1
	s_mov_b64 s[16:17], 0
	s_waitcnt vmcnt(0)
	v_cmp_lt_u32_e32 vcc, v1, v4
	s_and_saveexec_b64 s[14:15], vcc
	s_cbranch_execz .LBB0_1620
	s_add_u32 s12, s28, 0x200
	s_addc_u32 s13, s29, 0
	s_mov_b32 s3, 1
	s_branch .LBB0_1613

; __device__ __forceinline__ unsigned xb_add(unsigned* p, unsigned v) { return __hip_atomic_fetch_add(p, v, __ATOMIC_RELAXED, __HIP_MEMORY_SCOPE_AGENT); }
; __device__ __forceinline__ void xcd_barrier(const XcdBarrier& b, const bool xb_leader) {
;     ...
;             __builtin_amdgcn_fence(__ATOMIC_ACQUIRE, "agent");
;             xb_add(&bar[XB_XGEN(b.x)], 1u);
;             asm volatile("s_waitcnt vmcnt(0)" ::: "memory");
.LBB0_1623:
	s_or_b64 exec, exec, s[6:7]
	s_mov_b64 s[6:7], exec
	v_mbcnt_lo_u32_b32 v0, s6, 0
	v_mbcnt_hi_u32_b32 v0, s7, v0
	v_cmp_eq_u32_e32 vcc, 0, v0
	s_waitcnt vmcnt(0)
	s_and_saveexec_b64 s[10:11], vcc
	s_cbranch_execz .LBB0_1625
	s_bcnt1_i32_b64 s3, s[6:7]
	v_mov_b32_e32 v0, 0x2000
	v_mov_b32_e32 v1, s3
.LBB0_1625:
	s_or_b64 exec, exec, s[10:11]
	s_waitcnt vmcnt(0)

; __device__ __forceinline__ unsigned xb_add(unsigned* p, unsigned v) { return __hip_atomic_fetch_add(p, v, __ATOMIC_RELAXED, __HIP_MEMORY_SCOPE_AGENT); }
; __device__ __forceinline__ void xcd_barrier(const XcdBarrier& b, const bool xb_leader) {
;     ...
;             __builtin_amdgcn_fence(__ATOMIC_ACQUIRE, "agent");
;             xb_add(&bar[XB_XGEN(b.x)], 1u);
;             asm volatile("s_waitcnt vmcnt(0)" ::: "memory");
.LBB0_1730:
	s_or_b64 exec, exec, s[6:7]
	s_mov_b64 s[6:7], exec
	v_mbcnt_lo_u32_b32 v0, s6, 0
	v_mbcnt_hi_u32_b32 v0, s7, v0
	v_cmp_eq_u32_e32 vcc, 0, v0
	s_waitcnt vmcnt(0)
	s_and_saveexec_b64 s[10:11], vcc
	s_cbranch_execz .LBB0_1732
	s_bcnt1_i32_b64 s3, s[6:7]
	v_mov_b32_e32 v0, 0x2000
	v_mov_b32_e32 v1, s3
.LBB0_1732:
	s_or_b64 exec, exec, s[10:11]
	s_waitcnt vmcnt(0)

; __device__ __forceinline__ unsigned xb_add(unsigned* p, unsigned v) { return __hip_atomic_fetch_add(p, v, __ATOMIC_RELAXED, __HIP_MEMORY_SCOPE_AGENT); }
; __device__ __forceinline__ void xcd_barrier(const XcdBarrier& b, const bool xb_leader) {
;     ...
;             __builtin_amdgcn_fence(__ATOMIC_ACQUIRE, "agent");
;             xb_add(&bar[XB_XGEN(b.x)], 1u);
;             asm volatile("s_waitcnt vmcnt(0)" ::: "memory");
.LBB0_1827:
	s_or_b64 exec, exec, s[6:7]
	s_mov_b64 s[6:7], exec
	v_mbcnt_lo_u32_b32 v0, s6, 0
	v_mbcnt_hi_u32_b32 v0, s7, v0
	v_cmp_eq_u32_e32 vcc, 0, v0
	s_waitcnt vmcnt(0)
	s_and_saveexec_b64 s[10:11], vcc
	s_cbranch_execz .LBB0_1829
	s_bcnt1_i32_b64 s3, s[6:7]
	v_mov_b32_e32 v0, 0x2000
	v_mov_b32_e32 v1, s3
.LBB0_1829:
	s_or_b64 exec, exec, s[10:11]
	s_waitcnt vmcnt(0)

; __device__ __forceinline__ unsigned xb_ld(unsigned* p)              { return __hip_atomic_load(p, __ATOMIC_RELAXED, __HIP_MEMORY_SCOPE_AGENT); }
; __device__ __forceinline__ unsigned xb_add(unsigned* p, unsigned v) { return __hip_atomic_fetch_add(p, v, __ATOMIC_RELAXED, __HIP_MEMORY_SCOPE_AGENT); }
; #define XB_SPIN(cond, bar) do { unsigned _sp = 0; while (cond) { __builtin_amdgcn_s_sleep(1); \
;     if ((++_sp & 255u) == 0u) { if (xb_ld(&(bar)[XB_TMO])) break; if (_sp > XB_SPIN_CAP) { atomicAdd(&(bar)[XB_TMO], 1u); break; } } } } while (0)
; __device__ __forceinline__ void xcd_barrier(const XcdBarrier& b, const bool xb_leader) {
;     ...
;         const unsigned old = xb_add(&bar[XB_XSUB(b.x)], 1u);
;         const unsigned gen = old / nloc;
;         if (old + 1u == (gen + 1u) * nloc) {
;             __builtin_amdgcn_fence(__ATOMIC_RELEASE, "agent");
;             asm volatile("s_waitcnt vmcnt(0)" ::: "memory");
;             const unsigned og = xb_add(&bar[XB_TOP], 1u);
;             const unsigned tg = og / nx;
;             if (og + 1u == (tg + 1u) * nx) xb_add(&bar[XB_TOPGEN], 1u);
;             else XB_SPIN(xb_ld(&bar[XB_TOPGEN]) == tg, bar);
;             __builtin_amdgcn_fence(__ATOMIC_ACQUIRE, "agent");
;             xb_add(&bar[XB_XGEN(b.x)], 1u);
;             asm volatile("s_waitcnt vmcnt(0)" ::: "memory");
;         } else {
;             XB_SPIN(xb_ld(&bar[XB_XGEN(b.x)]) == gen, bar);
;             __builtin_amdgcn_fence(__ATOMIC_ACQUIRE, "agent");
;             asm volatile("s_waitcnt vmcnt(0)" ::: "memory");
;         }
.LBB0_1908:
	s_or_b64 exec, exec, s[8:9]
	v_cvt_f32_u32_e32 v2, v9
	s_waitcnt vmcnt(0)
	v_readfirstlane_b32 s2, v1
	v_sub_u32_e32 v1, 0, v9
	v_rcp_iflag_f32_e32 v2, v2
	v_add_u32_e32 v3, s2, v0
	v_mul_f32_e32 v2, 0x4f7ffffe, v2
	v_cvt_u32_f32_e32 v2, v2
	v_mul_lo_u32 v0, v1, v2
	v_mul_hi_u32 v0, v2, v0
	v_add_u32_e32 v0, v2, v0
	v_mul_hi_u32 v0, v3, v0
	v_mul_lo_u32 v1, v0, v9
	v_sub_u32_e32 v1, v3, v1
	v_add_u32_e32 v2, 1, v0
	v_cmp_ge_u32_e32 vcc, v1, v9
	s_nop 1
	v_cndmask_b32_e32 v0, v0, v2, vcc
	v_sub_u32_e32 v2, v1, v9
	v_cndmask_b32_e32 v1, v1, v2, vcc
	v_add_u32_e32 v2, 1, v0
	v_cmp_ge_u32_e32 vcc, v1, v9
	v_add_u32_e32 v1, 1, v3
	s_nop 0
	v_cndmask_b32_e32 v0, v0, v2, vcc
	v_mul_lo_u32 v2, v9, v0
	v_add_u32_e32 v2, v2, v9
	v_cmp_ne_u32_e32 vcc, v1, v2
	s_and_saveexec_b64 s[2:3], vcc
	s_xor_b64 s[2:3], exec, s[2:3]
	s_cbranch_execz .LBB0_1922
	s_waitcnt lgkmcnt(0)
	v_add_u32_e32 v0, 1, v0
	v_mul_lo_u32 v0, v0, v8
	v_mov_b32_e32 v1, 0x3000
	global_load_dword v1, v1, s[28:29] offset:1024 sc1
	s_add_u32 s12, s28, 0x3400
	s_addc_u32 s13, s29, 0
	s_waitcnt vmcnt(0)
	v_cmp_lt_u32_e32 vcc, v1, v0
	s_and_saveexec_b64 s[8:9], vcc
	s_cbranch_execz .LBB0_1921
	s_mov_b32 s26, 1
	s_mov_b64 s[14:15], 0
	v_mov_b32_e32 v1, 0
	s_branch .LBB0_1912

; __device__ __forceinline__ unsigned xb_ld(unsigned* p)              { return __hip_atomic_load(p, __ATOMIC_RELAXED, __HIP_MEMORY_SCOPE_AGENT); }
; __device__ __forceinline__ unsigned xb_add(unsigned* p, unsigned v) { return __hip_atomic_fetch_add(p, v, __ATOMIC_RELAXED, __HIP_MEMORY_SCOPE_AGENT); }
; #define XB_SPIN(cond, bar) do { unsigned _sp = 0; while (cond) { __builtin_amdgcn_s_sleep(1); \
;     if ((++_sp & 255u) == 0u) { if (xb_ld(&(bar)[XB_TMO])) break; if (_sp > XB_SPIN_CAP) { atomicAdd(&(bar)[XB_TMO], 1u); break; } } } } while (0)
; __device__ __forceinline__ void xcd_barrier(const XcdBarrier& b, const bool xb_leader) {
;     ...
;             else XB_SPIN(xb_ld(&bar[XB_TOPGEN]) == tg, bar);
;             __builtin_amdgcn_fence(__ATOMIC_ACQUIRE, "agent");
;             xb_add(&bar[XB_XGEN(b.x)], 1u);
;             asm volatile("s_waitcnt vmcnt(0)" ::: "memory");
;         } else {
;             XB_SPIN(xb_ld(&bar[XB_XGEN(b.x)]) == gen, bar);
.LBB0_1916:
	global_load_dword v2, v1, s[12:13] sc1
	s_add_i32 s26, s26, 1
	s_mov_b64 s[22:23], -1
	s_waitcnt vmcnt(0)
	v_cmp_ge_u32_e32 vcc, v2, v0
	s_orn2_b64 s[20:21], vcc, exec
	s_branch .LBB0_1911

; __device__ __forceinline__ unsigned xb_ld(unsigned* p)              { return __hip_atomic_load(p, __ATOMIC_RELAXED, __HIP_MEMORY_SCOPE_AGENT); }
; __device__ __forceinline__ unsigned xb_add(unsigned* p, unsigned v) { return __hip_atomic_fetch_add(p, v, __ATOMIC_RELAXED, __HIP_MEMORY_SCOPE_AGENT); }
; #define XB_SPIN(cond, bar) do { unsigned _sp = 0; while (cond) { __builtin_amdgcn_s_sleep(1); \
;     if ((++_sp & 255u) == 0u) { if (xb_ld(&(bar)[XB_TMO])) break; if (_sp > XB_SPIN_CAP) { atomicAdd(&(bar)[XB_TMO], 1u); break; } } } } while (0)
; __device__ __forceinline__ void xcd_barrier(const XcdBarrier& b, const bool xb_leader) {
;     ...
;         const unsigned old = xb_add(&bar[XB_XSUB(b.x)], 1u);
;         const unsigned gen = old / nloc;
;         if (old + 1u == (gen + 1u) * nloc) {
;             __builtin_amdgcn_fence(__ATOMIC_RELEASE, "agent");
;             asm volatile("s_waitcnt vmcnt(0)" ::: "memory");
;             const unsigned og = xb_add(&bar[XB_TOP], 1u);
;             const unsigned tg = og / nx;
;             if (og + 1u == (tg + 1u) * nx) xb_add(&bar[XB_TOPGEN], 1u);
;             else XB_SPIN(xb_ld(&bar[XB_TOPGEN]) == tg, bar);
.LBB0_1925:
	s_or_b64 exec, exec, s[8:9]
	v_cvt_f32_u32_e32 v2, v8
	s_waitcnt vmcnt(0)
	v_readfirstlane_b32 s2, v1
	s_add_u32 s8, s28, 0x3400
	s_addc_u32 s9, s29, 0
	v_rcp_iflag_f32_e32 v2, v2
	v_add_u32_e32 v0, s2, v0
	v_add_u32_e32 v3, 1, v0
	s_mov_b64 s[12:13], 0
	v_mul_f32_e32 v1, 0x4f7ffffe, v2
	v_cvt_u32_f32_e32 v1, v1
	v_sub_u32_e32 v2, 0, v8
	v_mul_lo_u32 v2, v2, v1
	v_mul_hi_u32 v2, v1, v2
	v_add_u32_e32 v1, v1, v2
	v_mul_hi_u32 v1, v0, v1
	v_mul_lo_u32 v2, v1, v8
	v_sub_u32_e32 v0, v0, v2
	v_add_u32_e32 v4, 1, v1
	v_cmp_ge_u32_e32 vcc, v0, v8
	v_sub_u32_e32 v2, v0, v8
	s_nop 0
	v_cndmask_b32_e32 v1, v1, v4, vcc
	v_cndmask_b32_e32 v0, v0, v2, vcc
	v_add_u32_e32 v2, 1, v1
	v_cmp_ge_u32_e32 vcc, v0, v8
	s_nop 1
	v_cndmask_b32_e32 v2, v1, v2, vcc
	v_mul_lo_u32 v0, v8, v2
	v_add_u32_e32 v0, v0, v8
	v_cmp_ne_u32_e32 vcc, v3, v0
	v_mov_b32_e32 v4, v0
	v_mov_b64_e32 v[0:1], s[8:9]
	s_and_saveexec_b64 s[2:3], vcc
	s_cbranch_execz .LBB0_1937
	v_mov_b32_e32 v0, 0
	global_load_dword v1, v0, s[8:9] sc1
	s_mov_b64 s[16:17], 0
	s_waitcnt vmcnt(0)
	v_cmp_lt_u32_e32 vcc, v1, v4
	s_and_saveexec_b64 s[14:15], vcc
	s_cbranch_execz .LBB0_1936
	s_add_u32 s12, s28, 0x200
	s_addc_u32 s13, s29, 0
	s_mov_b32 s28, 1
	s_branch .LBB0_1929

; __device__ __forceinline__ unsigned xb_ld(unsigned* p)              { return __hip_atomic_load(p, __ATOMIC_RELAXED, __HIP_MEMORY_SCOPE_AGENT); }
; #define XB_SPIN(cond, bar) do { unsigned _sp = 0; while (cond) { __builtin_amdgcn_s_sleep(1); \
;     if ((++_sp & 255u) == 0u) { if (xb_ld(&(bar)[XB_TMO])) break; if (_sp > XB_SPIN_CAP) { atomicAdd(&(bar)[XB_TMO], 1u); break; } } } } while (0)
; __device__ __forceinline__ void xcd_barrier(const XcdBarrier& b, const bool xb_leader) {
;     ...
;             else XB_SPIN(xb_ld(&bar[XB_TOPGEN]) == tg, bar);
.LBB0_1933:
	global_load_dword v1, v0, s[8:9] sc1
	s_add_i32 s28, s28, 1
	s_mov_b64 s[22:23], -1
	s_waitcnt vmcnt(0)
	v_cmp_ge_u32_e32 vcc, v1, v4
	s_orn2_b64 s[26:27], vcc, exec
	s_branch .LBB0_1928

; __device__ __forceinline__ unsigned xb_add(unsigned* p, unsigned v) { return __hip_atomic_fetch_add(p, v, __ATOMIC_RELAXED, __HIP_MEMORY_SCOPE_AGENT); }
; __device__ __forceinline__ void xcd_barrier(const XcdBarrier& b, const bool xb_leader) {
;     ...
;             __builtin_amdgcn_fence(__ATOMIC_ACQUIRE, "agent");
;             xb_add(&bar[XB_XGEN(b.x)], 1u);
;             asm volatile("s_waitcnt vmcnt(0)" ::: "memory");
.LBB0_1939:
	s_or_b64 exec, exec, s[2:3]
	s_mov_b64 s[2:3], exec
	v_mbcnt_lo_u32_b32 v0, s2, 0
	v_mbcnt_hi_u32_b32 v0, s3, v0
	v_cmp_eq_u32_e32 vcc, 0, v0
	s_waitcnt vmcnt(0)
	s_and_saveexec_b64 s[8:9], vcc
	s_cbranch_execz .LBB0_1941
	s_bcnt1_i32_b64 s2, s[2:3]
	v_mov_b32_e32 v0, 0x2000
	v_mov_b32_e32 v1, s2
.LBB0_1941:
	s_or_b64 exec, exec, s[8:9]
	s_waitcnt vmcnt(0)
